# T11 residual-epilogue de-serialisation: 7 of 8 second-half base loads of the bf16 residual epilogues (down L0, out-proj L1) issued with the first half's loads into dead registers; waits re-derived (on
# baseline (speedup 1.0000x reference)
;     __device__ __forceinline__ void operator()(const f32x4 (&acc)[2][2][4][2], const Unit& u, int wr, int wc, int fr, int fq) const {
;         const int row0 = u.pm * BM + wr * 64 + fr, col0 = u.pn * BM + wc * 32 + 8 * fq;
;         const float* __restrict__ gp = gate + (size_t)(u.pm >> 3) * 12288 + col0;
;         bf16_t* __restrict__ op = out + (size_t)row0 * 2048 + col0;
;         f32x4 gv[2][2];
; #pragma unroll
;         for (int bj = 0; bj < 2; ++bj)
; #pragma unroll
;             for (int n = 0; n < 2; ++n) gv[bj][n] = *(const f32x4*)(gp + bj * HALF + n * 4);
; #pragma unroll
;         for (int ai = 0; ai < 2; ++ai) {
;             if constexpr (BASE_F32) {
;                 const float* __restrict__ bp = (const float*)base + (size_t)row0 * 2048 + col0;
;                 f32x4 bs[4][2][2];
; #pragma unroll
;                 for (int m = 0; m < 4; ++m)
; #pragma unroll
;                     for (int bj = 0; bj < 2; ++bj)
; #pragma unroll
;                         for (int n = 0; n < 2; ++n) bs[m][bj][n] = *(const f32x4*)(bp + (size_t)(ai * HALF + m * 16) * 2048 + bj * HALF + n * 4);
; #pragma unroll
;                 for (int m = 0; m < 4; ++m)
; #pragma unroll
;                     for (int bj = 0; bj < 2; ++bj) { const f32x4 v0 = bs[m][bj][0] + gv[bj][0] * acc[ai][bj][m][0], v1 = bs[m][bj][1] + gv[bj][1] * acc[ai][bj][m][1];
;                         u32x4 w; w.x = cvt_pk_bf16(v0[0], v0[1]); w.y = cvt_pk_bf16(v0[2], v0[3]); w.z = cvt_pk_bf16(v1[0], v1[1]); w.w = cvt_pk_bf16(v1[2], v1[3]);
;                         *(u32x4*)(op + (size_t)(ai * HALF + m * 16) * 2048 + bj * HALF) = w; }
;             } else {
;                 const bf16_t* __restrict__ bp = (const bf16_t*)base + (size_t)row0 * 2048 + col0;
;                 u32x4 bs[4][2];
; #pragma unroll
;                 for (int m = 0; m < 4; ++m)
; #pragma unroll
;                     for (int bj = 0; bj < 2; ++bj) bs[m][bj] = *(const u32x4*)(bp + (size_t)(ai * HALF + m * 16) * 2048 + bj * HALF);
; #pragma unroll
;                 for (int m = 0; m < 4; ++m)
; #pragma unroll
;                     for (int bj = 0; bj < 2; ++bj) { const u32x4 b = bs[m][bj]; const f32x4 a0 = acc[ai][bj][m][0], a1 = acc[ai][bj][m][1], g0 = gv[bj][0], g1 = gv[bj][1];
;                         u32x4 w;
.LBB0_954:
	v_lshl_add_u32 v130, s46, 8, v174
	v_lshl_or_b32 v132, s47, 8, v176
	v_ashrrev_i32_e32 v131, 31, v130
	v_ashrrev_i32_e32 v133, 31, v132
	v_lshlrev_b64 v[146:147], 12, v[130:131]
	s_ashr_i32 s14, s46, 3
	v_lshlrev_b64 v[148:149], 1, v[132:133]
	v_lshl_add_u64 v[130:131], s[66:67], 0, v[146:147]
	s_mul_hi_i32 s15, s14, 0xc000
	s_mul_i32 s14, s14, 0xc000
	v_lshl_add_u64 v[172:173], v[130:131], 0, v[148:149]
	s_add_u32 s14, s30, s14
	s_addc_u32 s15, s31, s15
	v_add_co_u32_e32 v150, vcc, s29, v172
	global_load_dwordx4 v[180:183], v[172:173], off
	global_load_dwordx4 v[190:193], v[172:173], off offset:256
	v_lshl_add_u64 v[130:131], v[132:133], 2, s[14:15]
	v_addc_co_u32_e32 v151, vcc, 0, v173, vcc
	global_load_dwordx4 v[142:145], v[130:131], off
	global_load_dwordx4 v[138:141], v[130:131], off offset:16
	global_load_dwordx4 v[134:137], v[130:131], off offset:512
	s_nop 0
	global_load_dwordx4 v[130:133], v[130:131], off offset:528
	v_readlane_b32 s14, v247, 30
	global_load_dwordx4 v[194:197], v[150:151], off
	global_load_dwordx4 v[198:201], v[150:151], off offset:256
	v_add_co_u32_e32 v254, vcc, s40, v172
	s_nop 1
	v_addc_co_u32_e32 v255, vcc, 0, v173, vcc
	global_load_dwordx4 v[222:225], v[254:255], off
	global_load_dwordx4 v[226:229], v[254:255], off offset:256
	v_add_co_u32_e32 v254, vcc, s41, v172
	s_nop 1
	v_addc_co_u32_e32 v255, vcc, 0, v173, vcc
	global_load_dwordx4 v[230:233], v[254:255], off
	global_load_dwordx4 v[234:237], v[254:255], off offset:256
	v_add_co_u32_e32 v254, vcc, s42, v172
	s_nop 1
	v_addc_co_u32_e32 v255, vcc, 0, v173, vcc
	global_load_dwordx4 v[238:241], v[254:255], off
	global_load_dwordx4 v[242:245], v[254:255], off offset:256
	v_add_co_u32_e32 v254, vcc, s43, v172
	s_nop 1
	v_addc_co_u32_e32 v255, vcc, 0, v173, vcc
	global_load_dwordx4 v[250:253], v[254:255], off
	v_readlane_b32 s15, v247, 31
	s_waitcnt vmcnt(7)
	v_lshlrev_b32_e32 v184, 16, v180
	v_lshl_add_u64 v[146:147], s[14:15], 0, v[146:147]
	v_lshl_add_u64 v[170:171], v[146:147], 0, v[148:149]
	v_add_co_u32_e32 v146, vcc, s38, v172
	v_lshlrev_b32_e32 v218, 16, v191
	s_nop 0
	v_addc_co_u32_e32 v147, vcc, 0, v173, vcc
	v_add_co_u32_e32 v148, vcc, s39, v172
	v_fmac_f32_e32 v218, v120, v136
	s_nop 0
	v_addc_co_u32_e32 v149, vcc, 0, v173, vcc
	global_load_dwordx4 v[202:205], v[146:147], off
	global_load_dwordx4 v[206:209], v[146:147], off offset:256
	global_load_dwordx4 v[150:153], v[148:149], off
	s_nop 0
	global_load_dwordx4 v[146:149], v[148:149], off offset:256
	v_lshlrev_b32_e32 v120, 16, v195
	v_fmac_f32_e32 v120, v112, v144
	v_lshlrev_b32_e32 v112, 16, v196
	v_and_b32_e32 v180, 0xffff0000, v180
	v_lshlrev_b32_e32 v185, 16, v181
	v_and_b32_e32 v181, 0xffff0000, v181
	v_lshlrev_b32_e32 v189, 16, v182
	v_and_b32_e32 v182, 0xffff0000, v182
	v_lshlrev_b32_e32 v216, 16, v183
	v_and_b32_e32 v183, 0xffff0000, v183
	v_lshlrev_b32_e32 v217, 16, v190
	v_and_b32_e32 v190, 0xffff0000, v190
	v_and_b32_e32 v191, 0xffff0000, v191
	v_lshlrev_b32_e32 v219, 16, v192
	v_and_b32_e32 v192, 0xffff0000, v192
	v_lshlrev_b32_e32 v220, 16, v193
	v_and_b32_e32 v193, 0xffff0000, v193
	v_fmac_f32_e32 v112, v106, v138
	v_and_b32_e32 v106, 0xffff0000, v196
	v_fmac_f32_e32 v184, v126, v142
	v_fmac_f32_e32 v180, v127, v143
	v_fmac_f32_e32 v185, v128, v144
	v_fmac_f32_e32 v181, v129, v145
	v_fmac_f32_e32 v189, v122, v138
	v_fmac_f32_e32 v182, v123, v139
	v_fmac_f32_e32 v216, v124, v140
	v_fmac_f32_e32 v183, v125, v141
	v_fmac_f32_e32 v217, v118, v134
	v_fmac_f32_e32 v190, v119, v135
	v_fmac_f32_e32 v191, v121, v137
	v_fmac_f32_e32 v219, v114, v130
	v_fmac_f32_e32 v192, v115, v131
	v_fmac_f32_e32 v220, v116, v132
	v_fmac_f32_e32 v193, v117, v133
	v_lshlrev_b32_e32 v118, 16, v194
	v_and_b32_e32 v119, 0xffff0000, v194
	v_and_b32_e32 v121, 0xffff0000, v195
	v_cvt_pk_bf16_f32 v114, v184, v180
	v_cvt_pk_bf16_f32 v115, v185, v181
	v_cvt_pk_bf16_f32 v116, v189, v182
	v_cvt_pk_bf16_f32 v117, v216, v183
	v_fmac_f32_e32 v106, v107, v139
	v_fmac_f32_e32 v118, v110, v142
	v_fmac_f32_e32 v119, v111, v143
	global_store_dwordx4 v[170:171], v[114:117], off
	v_fmac_f32_e32 v121, v113, v145
	v_and_b32_e32 v107, 0xffff0000, v197
	v_cvt_pk_bf16_f32 v114, v217, v190
	v_cvt_pk_bf16_f32 v115, v218, v191
	v_cvt_pk_bf16_f32 v116, v219, v192
	v_cvt_pk_bf16_f32 v117, v220, v193
	global_store_dwordx4 v[170:171], v[114:117], off offset:256
	v_cvt_pk_bf16_f32 v110, v118, v119
	v_cvt_pk_bf16_f32 v111, v120, v121
	v_cvt_pk_bf16_f32 v112, v112, v106
	v_lshlrev_b32_e32 v106, 16, v197
	v_fmac_f32_e32 v106, v108, v140
	v_lshlrev_b32_e32 v108, 16, v198
	v_fmac_f32_e32 v108, v102, v134
	v_and_b32_e32 v102, 0xffff0000, v198
	v_fmac_f32_e32 v102, v103, v135
	v_lshlrev_b32_e32 v103, 16, v199
	v_fmac_f32_e32 v107, v109, v141
	v_cvt_pk_bf16_f32 v113, v106, v107
	v_add_co_u32_e32 v106, vcc, s29, v170
	v_fmac_f32_e32 v103, v104, v136
	v_and_b32_e32 v104, 0xffff0000, v199
	v_addc_co_u32_e32 v107, vcc, 0, v171, vcc
	v_fmac_f32_e32 v104, v105, v137
	global_store_dwordx4 v[106:107], v[110:113], off
	v_cvt_pk_bf16_f32 v102, v108, v102
	v_cvt_pk_bf16_f32 v103, v103, v104
	v_lshlrev_b32_e32 v104, 16, v200
	v_fmac_f32_e32 v104, v94, v130
	v_and_b32_e32 v94, 0xffff0000, v200
	v_fmac_f32_e32 v94, v95, v131
	v_cvt_pk_bf16_f32 v104, v104, v94
	v_lshlrev_b32_e32 v94, 16, v201
	v_and_b32_e32 v95, 0xffff0000, v201
	v_fmac_f32_e32 v94, v96, v132
	v_fmac_f32_e32 v95, v97, v133
	v_cvt_pk_bf16_f32 v105, v94, v95
	s_waitcnt vmcnt(6)
; __device__ __forceinline__ unsigned cvt_pk_bf16(float lo, float hi) { unsigned r; asm volatile("v_cvt_pk_bf16_f32 %0, %1, %2" : "=v"(r) : "v"(lo), "v"(hi)); return r; }
;     __device__ __forceinline__ void operator()(const f32x4 (&acc)[2][2][4][2], const Unit& u, int wr, int wc, int fr, int fq) const {
;     ...
;                     for (int bj = 0; bj < 2; ++bj) bs[m][bj] = *(const u32x4*)(bp + (size_t)(ai * HALF + m * 16) * 2048 + bj * HALF);
; #pragma unroll
;                 for (int m = 0; m < 4; ++m)
; #pragma unroll
;                     for (int bj = 0; bj < 2; ++bj) { const u32x4 b = bs[m][bj]; const f32x4 a0 = acc[ai][bj][m][0], a1 = acc[ai][bj][m][1], g0 = gv[bj][0], g1 = gv[bj][1];
;                         u32x4 w;
;                         w.x = cvt_pk_bf16(__builtin_bit_cast(float, b.x << 16) + g0[0] * a0[0], __builtin_bit_cast(float, b.x & 0xffff0000u) + g0[1] * a0[1]);
;                         w.y = cvt_pk_bf16(__builtin_bit_cast(float, b.y << 16) + g0[2] * a0[2], __builtin_bit_cast(float, b.y & 0xffff0000u) + g0[3] * a0[3]);
;                         w.z = cvt_pk_bf16(__builtin_bit_cast(float, b.z << 16) + g1[0] * a1[0], __builtin_bit_cast(float, b.z & 0xffff0000u) + g1[1] * a1[1]);
;                         w.w = cvt_pk_bf16(__builtin_bit_cast(float, b.w << 16) + g1[2] * a1[2], __builtin_bit_cast(float, b.w & 0xffff0000u) + g1[3] * a1[3]);
;                         *(u32x4*)(op + (size_t)(ai * HALF + m * 16) * 2048 + bj * HALF) = w; }
	v_lshlrev_b32_e32 v94, 16, v202
	v_and_b32_e32 v95, 0xffff0000, v202
	v_fmac_f32_e32 v94, v98, v142
	v_fmac_f32_e32 v95, v99, v143
	global_store_dwordx4 v[106:107], v[102:105], off offset:256
	v_cvt_pk_bf16_f32 v94, v94, v95
	v_lshlrev_b32_e32 v95, 16, v203
	v_and_b32_e32 v96, 0xffff0000, v203
	v_fmac_f32_e32 v95, v100, v144
	v_fmac_f32_e32 v96, v101, v145
	v_cvt_pk_bf16_f32 v95, v95, v96
	v_lshlrev_b32_e32 v96, 16, v204
	v_fmac_f32_e32 v96, v90, v138
	v_and_b32_e32 v90, 0xffff0000, v204
	v_fmac_f32_e32 v90, v91, v139
	v_cvt_pk_bf16_f32 v96, v96, v90
	v_lshlrev_b32_e32 v90, 16, v205
	v_fmac_f32_e32 v90, v92, v140
	s_waitcnt vmcnt(6)
	v_lshlrev_b32_e32 v92, 16, v206
	v_fmac_f32_e32 v92, v86, v134
	v_and_b32_e32 v86, 0xffff0000, v206
	v_and_b32_e32 v91, 0xffff0000, v205
	v_fmac_f32_e32 v86, v87, v135
	v_lshlrev_b32_e32 v87, 16, v207
	v_fmac_f32_e32 v91, v93, v141
	v_cvt_pk_bf16_f32 v97, v90, v91
	v_add_co_u32_e32 v90, vcc, s38, v170
	v_fmac_f32_e32 v87, v88, v136
	v_and_b32_e32 v88, 0xffff0000, v207
	v_addc_co_u32_e32 v91, vcc, 0, v171, vcc
	v_fmac_f32_e32 v88, v89, v137
	global_store_dwordx4 v[90:91], v[94:97], off
	v_cvt_pk_bf16_f32 v86, v92, v86
	v_cvt_pk_bf16_f32 v87, v87, v88
	v_lshlrev_b32_e32 v88, 16, v208
	v_fmac_f32_e32 v88, v78, v130
	v_and_b32_e32 v78, 0xffff0000, v208
	v_fmac_f32_e32 v78, v79, v131
	v_cvt_pk_bf16_f32 v88, v88, v78
	v_lshlrev_b32_e32 v78, 16, v209
	v_and_b32_e32 v79, 0xffff0000, v209
	v_fmac_f32_e32 v78, v80, v132
	v_fmac_f32_e32 v79, v81, v133
	v_cvt_pk_bf16_f32 v89, v78, v79
	s_waitcnt vmcnt(6)
	v_lshlrev_b32_e32 v78, 16, v150
	v_and_b32_e32 v79, 0xffff0000, v150
	v_fmac_f32_e32 v78, v82, v142
	v_fmac_f32_e32 v79, v83, v143
	global_store_dwordx4 v[90:91], v[86:89], off offset:256
	v_cvt_pk_bf16_f32 v78, v78, v79
	v_lshlrev_b32_e32 v79, 16, v151
	v_and_b32_e32 v80, 0xffff0000, v151
	v_fmac_f32_e32 v79, v84, v144
	v_fmac_f32_e32 v80, v85, v145
	v_cvt_pk_bf16_f32 v79, v79, v80
	v_lshlrev_b32_e32 v80, 16, v152
	v_fmac_f32_e32 v80, v74, v138
	v_and_b32_e32 v74, 0xffff0000, v152
	v_fmac_f32_e32 v74, v75, v139
	v_cvt_pk_bf16_f32 v80, v80, v74
	v_lshlrev_b32_e32 v74, 16, v153
	v_fmac_f32_e32 v74, v76, v140
	s_waitcnt vmcnt(6)
	v_lshlrev_b32_e32 v76, 16, v146
	v_fmac_f32_e32 v76, v70, v134
	v_and_b32_e32 v70, 0xffff0000, v146
	v_and_b32_e32 v75, 0xffff0000, v153
	v_fmac_f32_e32 v70, v71, v135
	v_lshlrev_b32_e32 v71, 16, v147
	v_fmac_f32_e32 v75, v77, v141
	v_cvt_pk_bf16_f32 v81, v74, v75
	v_add_co_u32_e32 v74, vcc, s39, v170
	v_fmac_f32_e32 v71, v72, v136
	v_and_b32_e32 v72, 0xffff0000, v147
	v_addc_co_u32_e32 v75, vcc, 0, v171, vcc
	v_fmac_f32_e32 v72, v73, v137
	global_store_dwordx4 v[74:75], v[78:81], off
	v_cvt_pk_bf16_f32 v70, v76, v70
	v_cvt_pk_bf16_f32 v71, v71, v72
	v_lshlrev_b32_e32 v72, 16, v148
	v_fmac_f32_e32 v72, v66, v130
	v_and_b32_e32 v66, 0xffff0000, v148
	v_fmac_f32_e32 v66, v67, v131
	v_cvt_pk_bf16_f32 v72, v72, v66
	v_lshlrev_b32_e32 v66, 16, v149
	v_fmac_f32_e32 v66, v68, v132
	v_and_b32_e32 v67, 0xffff0000, v149
	v_fmac_f32_e32 v67, v69, v133
	v_cvt_pk_bf16_f32 v73, v66, v67
	global_store_dwordx4 v[74:75], v[70:73], off offset:256
	s_nop 1
	s_waitcnt vmcnt(8)
; __device__ __forceinline__ unsigned cvt_pk_bf16(float lo, float hi) { unsigned r; asm volatile("v_cvt_pk_bf16_f32 %0, %1, %2" : "=v"(r) : "v"(lo), "v"(hi)); return r; }
;     __device__ __forceinline__ void operator()(const f32x4 (&acc)[2][2][4][2], const Unit& u, int wr, int wc, int fr, int fq) const {
;     ...
;                     for (int bj = 0; bj < 2; ++bj) bs[m][bj] = *(const u32x4*)(bp + (size_t)(ai * HALF + m * 16) * 2048 + bj * HALF);
; #pragma unroll
;                 for (int m = 0; m < 4; ++m)
; #pragma unroll
;                     for (int bj = 0; bj < 2; ++bj) { const u32x4 b = bs[m][bj]; const f32x4 a0 = acc[ai][bj][m][0], a1 = acc[ai][bj][m][1], g0 = gv[bj][0], g1 = gv[bj][1];
;                         u32x4 w;
;                         w.x = cvt_pk_bf16(__builtin_bit_cast(float, b.x << 16) + g0[0] * a0[0], __builtin_bit_cast(float, b.x & 0xffff0000u) + g0[1] * a0[1]);
;                         w.y = cvt_pk_bf16(__builtin_bit_cast(float, b.y << 16) + g0[2] * a0[2], __builtin_bit_cast(float, b.y & 0xffff0000u) + g0[3] * a0[3]);
;                         w.z = cvt_pk_bf16(__builtin_bit_cast(float, b.z << 16) + g1[0] * a1[0], __builtin_bit_cast(float, b.z & 0xffff0000u) + g1[1] * a1[1]);
;                         w.w = cvt_pk_bf16(__builtin_bit_cast(float, b.w << 16) + g1[2] * a1[2], __builtin_bit_cast(float, b.w & 0xffff0000u) + g1[3] * a1[3]);
;                         *(u32x4*)(op + (size_t)(ai * HALF + m * 16) * 2048 + bj * HALF) = w; }
	v_lshlrev_b32_e32 v98, 16, v222
	v_fmac_f32_e32 v98, v62, v142
	s_nop 0
	v_add_co_u32_e32 v66, vcc, s43, v172
	v_and_b32_e32 v62, 0xffff0000, v222
	s_nop 0
	v_addc_co_u32_e32 v67, vcc, 0, v173, vcc
	s_nop 0
	global_load_dwordx4 v[66:69], v[66:67], off offset:256
	v_fmac_f32_e32 v62, v63, v143
	v_lshlrev_b32_e32 v63, 16, v223
	v_fmac_f32_e32 v63, v64, v144
	v_and_b32_e32 v64, 0xffff0000, v223
	v_fmac_f32_e32 v64, v65, v145
	v_cvt_pk_bf16_f32 v62, v98, v62
	v_cvt_pk_bf16_f32 v63, v63, v64
	v_lshlrev_b32_e32 v64, 16, v224
	v_fmac_f32_e32 v64, v58, v138
	v_and_b32_e32 v58, 0xffff0000, v224
	v_fmac_f32_e32 v58, v59, v139
	v_cvt_pk_bf16_f32 v64, v64, v58
	v_lshlrev_b32_e32 v58, 16, v225
	v_fmac_f32_e32 v58, v60, v140
	v_lshlrev_b32_e32 v60, 16, v226
	v_fmac_f32_e32 v60, v54, v134
	v_and_b32_e32 v54, 0xffff0000, v226
	v_and_b32_e32 v59, 0xffff0000, v225
	v_fmac_f32_e32 v54, v55, v135
	v_lshlrev_b32_e32 v55, 16, v227
	v_fmac_f32_e32 v59, v61, v141
	v_cvt_pk_bf16_f32 v65, v58, v59
	v_add_co_u32_e32 v58, vcc, s40, v170
	v_fmac_f32_e32 v55, v56, v136
	v_and_b32_e32 v56, 0xffff0000, v227
	v_addc_co_u32_e32 v59, vcc, 0, v171, vcc
	v_fmac_f32_e32 v56, v57, v137
	global_store_dwordx4 v[58:59], v[62:65], off
	v_cvt_pk_bf16_f32 v54, v60, v54
	v_cvt_pk_bf16_f32 v55, v55, v56
	v_lshlrev_b32_e32 v56, 16, v228
	v_fmac_f32_e32 v56, v46, v130
	v_and_b32_e32 v46, 0xffff0000, v228
	v_fmac_f32_e32 v46, v47, v131
	v_cvt_pk_bf16_f32 v56, v56, v46
	v_lshlrev_b32_e32 v46, 16, v229
	v_and_b32_e32 v47, 0xffff0000, v229
	v_fmac_f32_e32 v46, v48, v132
	v_fmac_f32_e32 v47, v49, v133
	v_cvt_pk_bf16_f32 v57, v46, v47
	global_store_dwordx4 v[58:59], v[54:57], off offset:256
	v_lshlrev_b32_e32 v46, 16, v230
	v_and_b32_e32 v47, 0xffff0000, v230
	v_fmac_f32_e32 v46, v50, v142
	v_fmac_f32_e32 v47, v51, v143
	v_cvt_pk_bf16_f32 v46, v46, v47
	v_lshlrev_b32_e32 v47, 16, v231
	v_and_b32_e32 v48, 0xffff0000, v231
	v_fmac_f32_e32 v47, v52, v144
	v_fmac_f32_e32 v48, v53, v145
	v_cvt_pk_bf16_f32 v47, v47, v48
	v_lshlrev_b32_e32 v48, 16, v232
	v_fmac_f32_e32 v48, v42, v138
	v_and_b32_e32 v42, 0xffff0000, v232
	v_fmac_f32_e32 v42, v43, v139
	v_cvt_pk_bf16_f32 v48, v48, v42
	v_lshlrev_b32_e32 v42, 16, v233
	v_fmac_f32_e32 v42, v44, v140
	v_lshlrev_b32_e32 v44, 16, v234
	v_fmac_f32_e32 v44, v38, v134
	v_and_b32_e32 v38, 0xffff0000, v234
	v_and_b32_e32 v43, 0xffff0000, v233
	v_fmac_f32_e32 v38, v39, v135
	v_lshlrev_b32_e32 v39, 16, v235
	v_fmac_f32_e32 v43, v45, v141
	v_cvt_pk_bf16_f32 v49, v42, v43
	v_add_co_u32_e32 v42, vcc, s41, v170
	v_fmac_f32_e32 v39, v40, v136
	v_and_b32_e32 v40, 0xffff0000, v235
	v_addc_co_u32_e32 v43, vcc, 0, v171, vcc
	v_fmac_f32_e32 v40, v41, v137
	global_store_dwordx4 v[42:43], v[46:49], off
	v_cvt_pk_bf16_f32 v38, v44, v38
	v_cvt_pk_bf16_f32 v39, v39, v40
	v_lshlrev_b32_e32 v40, 16, v236
	v_fmac_f32_e32 v40, v30, v130
	v_and_b32_e32 v30, 0xffff0000, v236
	v_fmac_f32_e32 v30, v31, v131
	v_cvt_pk_bf16_f32 v40, v40, v30
	v_lshlrev_b32_e32 v30, 16, v237
	v_and_b32_e32 v31, 0xffff0000, v237
	v_fmac_f32_e32 v30, v32, v132
	v_fmac_f32_e32 v31, v33, v133
	v_cvt_pk_bf16_f32 v41, v30, v31
	v_lshlrev_b32_e32 v30, 16, v238
	v_and_b32_e32 v31, 0xffff0000, v238
	v_fmac_f32_e32 v30, v34, v142
	v_fmac_f32_e32 v31, v35, v143
	global_store_dwordx4 v[42:43], v[38:41], off offset:256
	v_cvt_pk_bf16_f32 v30, v30, v31
	v_lshlrev_b32_e32 v31, 16, v239
	v_and_b32_e32 v32, 0xffff0000, v239
	v_fmac_f32_e32 v31, v36, v144
	v_fmac_f32_e32 v32, v37, v145
	v_cvt_pk_bf16_f32 v31, v31, v32
	v_lshlrev_b32_e32 v32, 16, v240
	v_fmac_f32_e32 v32, v26, v138
	v_and_b32_e32 v26, 0xffff0000, v240
	v_fmac_f32_e32 v26, v27, v139
	v_cvt_pk_bf16_f32 v32, v32, v26
	v_lshlrev_b32_e32 v26, 16, v241
	v_fmac_f32_e32 v26, v28, v140
	v_lshlrev_b32_e32 v28, 16, v242
	v_fmac_f32_e32 v28, v22, v134
	v_and_b32_e32 v22, 0xffff0000, v242
	v_and_b32_e32 v27, 0xffff0000, v241
	v_fmac_f32_e32 v22, v23, v135
	v_lshlrev_b32_e32 v23, 16, v243
	v_fmac_f32_e32 v27, v29, v141
	v_cvt_pk_bf16_f32 v33, v26, v27
	v_add_co_u32_e32 v26, vcc, s42, v170
	v_fmac_f32_e32 v23, v24, v136
	v_and_b32_e32 v24, 0xffff0000, v243
	v_addc_co_u32_e32 v27, vcc, 0, v171, vcc
	v_fmac_f32_e32 v24, v25, v137
	global_store_dwordx4 v[26:27], v[30:33], off
	v_cvt_pk_bf16_f32 v22, v28, v22
	v_cvt_pk_bf16_f32 v23, v23, v24
	v_lshlrev_b32_e32 v24, 16, v244
	v_fmac_f32_e32 v24, v14, v130
	v_and_b32_e32 v14, 0xffff0000, v244
	v_fmac_f32_e32 v14, v15, v131
	v_cvt_pk_bf16_f32 v24, v24, v14
	v_lshlrev_b32_e32 v14, 16, v245
	v_and_b32_e32 v15, 0xffff0000, v245
	v_fmac_f32_e32 v14, v16, v132
	v_fmac_f32_e32 v15, v17, v133
	v_cvt_pk_bf16_f32 v25, v14, v15
	v_lshlrev_b32_e32 v14, 16, v250
	v_and_b32_e32 v15, 0xffff0000, v250
	v_fmac_f32_e32 v14, v18, v142
	v_fmac_f32_e32 v15, v19, v143
	global_store_dwordx4 v[26:27], v[22:25], off offset:256
	v_cvt_pk_bf16_f32 v14, v14, v15
	v_lshlrev_b32_e32 v15, 16, v251
	v_and_b32_e32 v16, 0xffff0000, v251
	v_fmac_f32_e32 v15, v20, v144
	v_fmac_f32_e32 v16, v21, v145
	v_cvt_pk_bf16_f32 v15, v15, v16
	v_lshlrev_b32_e32 v16, 16, v252
	v_fmac_f32_e32 v16, v10, v138
	v_and_b32_e32 v10, 0xffff0000, v252
	v_fmac_f32_e32 v10, v11, v139
	v_cvt_pk_bf16_f32 v16, v16, v10
	v_lshlrev_b32_e32 v10, 16, v253
	v_fmac_f32_e32 v10, v12, v140
	s_waitcnt vmcnt(6)
	v_lshlrev_b32_e32 v12, 16, v66
	v_fmac_f32_e32 v12, v6, v134
	v_and_b32_e32 v6, 0xffff0000, v66
	v_and_b32_e32 v11, 0xffff0000, v253
	v_fmac_f32_e32 v6, v7, v135
	v_lshlrev_b32_e32 v7, 16, v67
	v_fmac_f32_e32 v11, v13, v141
	v_cvt_pk_bf16_f32 v17, v10, v11
	v_add_co_u32_e32 v10, vcc, s43, v170
	v_fmac_f32_e32 v7, v8, v136
	v_and_b32_e32 v8, 0xffff0000, v67
	v_addc_co_u32_e32 v11, vcc, 0, v171, vcc
	v_fmac_f32_e32 v8, v9, v137
	global_store_dwordx4 v[10:11], v[14:17], off
	v_cvt_pk_bf16_f32 v6, v12, v6
	v_cvt_pk_bf16_f32 v7, v7, v8
	v_lshlrev_b32_e32 v8, 16, v68
	v_fmac_f32_e32 v8, v2, v130
	v_and_b32_e32 v2, 0xffff0000, v68
	v_fmac_f32_e32 v2, v3, v131
	v_cvt_pk_bf16_f32 v8, v8, v2
	v_lshlrev_b32_e32 v2, 16, v69
	v_and_b32_e32 v3, 0xffff0000, v69
	v_fmac_f32_e32 v2, v4, v132
	v_fmac_f32_e32 v3, v5, v133
	v_cvt_pk_bf16_f32 v9, v2, v3
	global_store_dwordx4 v[10:11], v[6:9], off offset:256
	s_and_b64 vcc, exec, s[2:3]
	s_mov_b64 s[2:3], -1
	s_cbranch_vccnz .LBB0_939
	s_andn2_b64 vcc, exec, s[6:7]
	s_cbranch_vccnz .LBB0_938
	s_barrier
	s_branch .LBB0_938

;     __device__ __forceinline__ void operator()(const f32x4 (&acc)[2][2][4][2], const Unit& u, int wr, int wc, int fr, int fq) const {
;         const int row0 = u.pm * BM + wr * 64 + fr, col0 = u.pn * BM + wc * 32 + 8 * fq;
;         const float* __restrict__ gp = gate + (size_t)(u.pm >> 3) * 12288 + col0;
;         bf16_t* __restrict__ op = out + (size_t)row0 * 2048 + col0;
;         f32x4 gv[2][2];
; #pragma unroll
;         for (int bj = 0; bj < 2; ++bj)
; #pragma unroll
;             for (int n = 0; n < 2; ++n) gv[bj][n] = *(const f32x4*)(gp + bj * HALF + n * 4);
; #pragma unroll
;         for (int ai = 0; ai < 2; ++ai) {
;             if constexpr (BASE_F32) {
;                 const float* __restrict__ bp = (const float*)base + (size_t)row0 * 2048 + col0;
;                 f32x4 bs[4][2][2];
; #pragma unroll
;                 for (int m = 0; m < 4; ++m)
; #pragma unroll
;                     for (int bj = 0; bj < 2; ++bj)
; #pragma unroll
;                         for (int n = 0; n < 2; ++n) bs[m][bj][n] = *(const f32x4*)(bp + (size_t)(ai * HALF + m * 16) * 2048 + bj * HALF + n * 4);
; #pragma unroll
;                 for (int m = 0; m < 4; ++m)
; #pragma unroll
;                     for (int bj = 0; bj < 2; ++bj) { const f32x4 v0 = bs[m][bj][0] + gv[bj][0] * acc[ai][bj][m][0], v1 = bs[m][bj][1] + gv[bj][1] * acc[ai][bj][m][1];
;                         u32x4 w; w.x = cvt_pk_bf16(v0[0], v0[1]); w.y = cvt_pk_bf16(v0[2], v0[3]); w.z = cvt_pk_bf16(v1[0], v1[1]); w.w = cvt_pk_bf16(v1[2], v1[3]);
;                         *(u32x4*)(op + (size_t)(ai * HALF + m * 16) * 2048 + bj * HALF) = w; }
;             } else {
;                 const bf16_t* __restrict__ bp = (const bf16_t*)base + (size_t)row0 * 2048 + col0;
;                 u32x4 bs[4][2];
; #pragma unroll
;                 for (int m = 0; m < 4; ++m)
; #pragma unroll
;                     for (int bj = 0; bj < 2; ++bj) bs[m][bj] = *(const u32x4*)(bp + (size_t)(ai * HALF + m * 16) * 2048 + bj * HALF);
; #pragma unroll
;                 for (int m = 0; m < 4; ++m)
; #pragma unroll
;                     for (int bj = 0; bj < 2; ++bj) { const u32x4 b = bs[m][bj]; const f32x4 a0 = acc[ai][bj][m][0], a1 = acc[ai][bj][m][1], g0 = gv[bj][0], g1 = gv[bj][1];
;                         u32x4 w;
.LBB0_1459:
	v_lshl_add_u32 v130, s18, 8, v1
	v_lshl_or_b32 v132, s49, 8, v175
	v_ashrrev_i32_e32 v131, 31, v130
	v_readlane_b32 s20, v247, 30
	v_ashrrev_i32_e32 v133, 31, v132
	v_lshlrev_b64 v[146:147], 12, v[130:131]
	v_readlane_b32 s21, v247, 31
	s_ashr_i32 s11, s18, 3
	v_lshlrev_b64 v[148:149], 1, v[132:133]
	v_lshl_add_u64 v[130:131], s[20:21], 0, v[146:147]
	s_mul_hi_i32 s13, s11, 0xc000
	s_mul_i32 s11, s11, 0xc000
	v_lshl_add_u64 v[172:173], v[130:131], 0, v[148:149]
	s_add_u32 s20, s36, s11
	s_addc_u32 s21, s37, s13
	v_add_co_u32_e32 v150, vcc, s35, v172
	global_load_dwordx4 v[180:183], v[172:173], off
	global_load_dwordx4 v[188:191], v[172:173], off offset:256
	v_lshl_add_u64 v[130:131], v[132:133], 2, s[20:21]
	v_addc_co_u32_e32 v151, vcc, 0, v173, vcc
	global_load_dwordx4 v[142:145], v[130:131], off
	global_load_dwordx4 v[138:141], v[130:131], off offset:16
	global_load_dwordx4 v[134:137], v[130:131], off offset:512
	s_nop 0
	global_load_dwordx4 v[130:133], v[130:131], off offset:528
	v_lshl_add_u64 v[146:147], s[66:67], 0, v[146:147]
	global_load_dwordx4 v[192:195], v[150:151], off
	global_load_dwordx4 v[196:199], v[150:151], off offset:256
	v_add_co_u32_e32 v254, vcc, s45, v172
	s_nop 1
	v_addc_co_u32_e32 v255, vcc, 0, v173, vcc
	global_load_dwordx4 v[222:225], v[254:255], off
	global_load_dwordx4 v[226:229], v[254:255], off offset:256
	v_add_co_u32_e32 v254, vcc, s46, v172
	s_nop 1
	v_addc_co_u32_e32 v255, vcc, 0, v173, vcc
	global_load_dwordx4 v[230:233], v[254:255], off
	global_load_dwordx4 v[234:237], v[254:255], off offset:256
	v_add_co_u32_e32 v254, vcc, s47, v172
	s_nop 1
	v_addc_co_u32_e32 v255, vcc, 0, v173, vcc
	global_load_dwordx4 v[238:241], v[254:255], off
	global_load_dwordx4 v[242:245], v[254:255], off offset:256
	v_add_co_u32_e32 v254, vcc, s48, v172
	s_nop 1
	v_addc_co_u32_e32 v255, vcc, 0, v173, vcc
	global_load_dwordx4 v[250:253], v[254:255], off
	v_lshl_add_u64 v[170:171], v[146:147], 0, v[148:149]
	v_add_co_u32_e32 v146, vcc, s44, v172
	s_waitcnt vmcnt(7)
	v_lshlrev_b32_e32 v179, 16, v180
	v_addc_co_u32_e32 v147, vcc, 0, v173, vcc
	v_add_co_u32_e32 v148, vcc, s41, v172
	v_lshlrev_b32_e32 v213, 16, v189
	s_nop 0
	v_addc_co_u32_e32 v149, vcc, 0, v173, vcc
	global_load_dwordx4 v[200:203], v[146:147], off
	global_load_dwordx4 v[204:207], v[146:147], off offset:256
	global_load_dwordx4 v[150:153], v[148:149], off
	s_nop 0
	global_load_dwordx4 v[146:149], v[148:149], off offset:256
	v_fmac_f32_e32 v213, v120, v136
	v_lshlrev_b32_e32 v120, 16, v193
	v_fmac_f32_e32 v120, v112, v144
	v_lshlrev_b32_e32 v112, 16, v194
	v_and_b32_e32 v180, 0xffff0000, v180
	v_lshlrev_b32_e32 v184, 16, v181
	v_and_b32_e32 v181, 0xffff0000, v181
	v_lshlrev_b32_e32 v185, 16, v182
	v_and_b32_e32 v182, 0xffff0000, v182
	v_lshlrev_b32_e32 v208, 16, v183
	v_and_b32_e32 v183, 0xffff0000, v183
	v_lshlrev_b32_e32 v209, 16, v188
	v_and_b32_e32 v188, 0xffff0000, v188
	v_and_b32_e32 v189, 0xffff0000, v189
	v_lshlrev_b32_e32 v214, 16, v190
	v_and_b32_e32 v190, 0xffff0000, v190
	v_lshlrev_b32_e32 v215, 16, v191
	v_and_b32_e32 v191, 0xffff0000, v191
	v_fmac_f32_e32 v112, v106, v138
	v_and_b32_e32 v106, 0xffff0000, v194
	v_fmac_f32_e32 v179, v126, v142
	v_fmac_f32_e32 v180, v127, v143
	v_fmac_f32_e32 v184, v128, v144
	v_fmac_f32_e32 v181, v129, v145
	v_fmac_f32_e32 v185, v122, v138
	v_fmac_f32_e32 v182, v123, v139
	v_fmac_f32_e32 v208, v124, v140
	v_fmac_f32_e32 v183, v125, v141
	v_fmac_f32_e32 v209, v118, v134
	v_fmac_f32_e32 v188, v119, v135
	v_fmac_f32_e32 v189, v121, v137
	v_fmac_f32_e32 v214, v114, v130
	v_fmac_f32_e32 v190, v115, v131
	v_fmac_f32_e32 v215, v116, v132
	v_fmac_f32_e32 v191, v117, v133
	v_lshlrev_b32_e32 v118, 16, v192
	v_and_b32_e32 v119, 0xffff0000, v192
	v_and_b32_e32 v121, 0xffff0000, v193
	v_cvt_pk_bf16_f32 v114, v179, v180
	v_cvt_pk_bf16_f32 v115, v184, v181
	v_cvt_pk_bf16_f32 v116, v185, v182
	v_cvt_pk_bf16_f32 v117, v208, v183
	v_fmac_f32_e32 v106, v107, v139
	v_fmac_f32_e32 v118, v110, v142
	v_fmac_f32_e32 v119, v111, v143
	global_store_dwordx4 v[170:171], v[114:117], off
	v_fmac_f32_e32 v121, v113, v145
	v_and_b32_e32 v107, 0xffff0000, v195
	v_cvt_pk_bf16_f32 v114, v209, v188
	v_cvt_pk_bf16_f32 v115, v213, v189
	v_cvt_pk_bf16_f32 v116, v214, v190
	v_cvt_pk_bf16_f32 v117, v215, v191
	global_store_dwordx4 v[170:171], v[114:117], off offset:256
	v_cvt_pk_bf16_f32 v110, v118, v119
	v_cvt_pk_bf16_f32 v111, v120, v121
	v_cvt_pk_bf16_f32 v112, v112, v106
	v_lshlrev_b32_e32 v106, 16, v195
	v_fmac_f32_e32 v106, v108, v140
	v_lshlrev_b32_e32 v108, 16, v196
	v_fmac_f32_e32 v108, v102, v134
	v_and_b32_e32 v102, 0xffff0000, v196
	v_fmac_f32_e32 v102, v103, v135
	v_lshlrev_b32_e32 v103, 16, v197
	v_fmac_f32_e32 v107, v109, v141
	v_cvt_pk_bf16_f32 v113, v106, v107
	v_add_co_u32_e32 v106, vcc, s35, v170
	v_fmac_f32_e32 v103, v104, v136
	v_and_b32_e32 v104, 0xffff0000, v197
	v_addc_co_u32_e32 v107, vcc, 0, v171, vcc
	v_fmac_f32_e32 v104, v105, v137
	global_store_dwordx4 v[106:107], v[110:113], off
	v_cvt_pk_bf16_f32 v102, v108, v102
	v_cvt_pk_bf16_f32 v103, v103, v104
	v_lshlrev_b32_e32 v104, 16, v198
	v_fmac_f32_e32 v104, v94, v130
	v_and_b32_e32 v94, 0xffff0000, v198
	v_fmac_f32_e32 v94, v95, v131
	v_cvt_pk_bf16_f32 v104, v104, v94
	v_lshlrev_b32_e32 v94, 16, v199
	v_and_b32_e32 v95, 0xffff0000, v199
	v_fmac_f32_e32 v94, v96, v132
	v_fmac_f32_e32 v95, v97, v133
	v_cvt_pk_bf16_f32 v105, v94, v95
	s_waitcnt vmcnt(6)
; __device__ __forceinline__ unsigned cvt_pk_bf16(float lo, float hi) { unsigned r; asm volatile("v_cvt_pk_bf16_f32 %0, %1, %2" : "=v"(r) : "v"(lo), "v"(hi)); return r; }
;     __device__ __forceinline__ void operator()(const f32x4 (&acc)[2][2][4][2], const Unit& u, int wr, int wc, int fr, int fq) const {
;     ...
;                     for (int bj = 0; bj < 2; ++bj) bs[m][bj] = *(const u32x4*)(bp + (size_t)(ai * HALF + m * 16) * 2048 + bj * HALF);
; #pragma unroll
;                 for (int m = 0; m < 4; ++m)
; #pragma unroll
;                     for (int bj = 0; bj < 2; ++bj) { const u32x4 b = bs[m][bj]; const f32x4 a0 = acc[ai][bj][m][0], a1 = acc[ai][bj][m][1], g0 = gv[bj][0], g1 = gv[bj][1];
;                         u32x4 w;
;                         w.x = cvt_pk_bf16(__builtin_bit_cast(float, b.x << 16) + g0[0] * a0[0], __builtin_bit_cast(float, b.x & 0xffff0000u) + g0[1] * a0[1]);
;                         w.y = cvt_pk_bf16(__builtin_bit_cast(float, b.y << 16) + g0[2] * a0[2], __builtin_bit_cast(float, b.y & 0xffff0000u) + g0[3] * a0[3]);
;                         w.z = cvt_pk_bf16(__builtin_bit_cast(float, b.z << 16) + g1[0] * a1[0], __builtin_bit_cast(float, b.z & 0xffff0000u) + g1[1] * a1[1]);
;                         w.w = cvt_pk_bf16(__builtin_bit_cast(float, b.w << 16) + g1[2] * a1[2], __builtin_bit_cast(float, b.w & 0xffff0000u) + g1[3] * a1[3]);
;                         *(u32x4*)(op + (size_t)(ai * HALF + m * 16) * 2048 + bj * HALF) = w; }
	v_lshlrev_b32_e32 v94, 16, v200
	v_and_b32_e32 v95, 0xffff0000, v200
	v_fmac_f32_e32 v94, v98, v142
	v_fmac_f32_e32 v95, v99, v143
	global_store_dwordx4 v[106:107], v[102:105], off offset:256
	v_cvt_pk_bf16_f32 v94, v94, v95
	v_lshlrev_b32_e32 v95, 16, v201
	v_and_b32_e32 v96, 0xffff0000, v201
	v_fmac_f32_e32 v95, v100, v144
	v_fmac_f32_e32 v96, v101, v145
	v_cvt_pk_bf16_f32 v95, v95, v96
	v_lshlrev_b32_e32 v96, 16, v202
	v_fmac_f32_e32 v96, v90, v138
	v_and_b32_e32 v90, 0xffff0000, v202
	v_fmac_f32_e32 v90, v91, v139
	v_cvt_pk_bf16_f32 v96, v96, v90
	v_lshlrev_b32_e32 v90, 16, v203
	v_fmac_f32_e32 v90, v92, v140
	s_waitcnt vmcnt(6)
	v_lshlrev_b32_e32 v92, 16, v204
	v_fmac_f32_e32 v92, v86, v134
	v_and_b32_e32 v86, 0xffff0000, v204
	v_and_b32_e32 v91, 0xffff0000, v203
	v_fmac_f32_e32 v86, v87, v135
	v_lshlrev_b32_e32 v87, 16, v205
	v_fmac_f32_e32 v91, v93, v141
	v_cvt_pk_bf16_f32 v97, v90, v91
	v_add_co_u32_e32 v90, vcc, s44, v170
	v_fmac_f32_e32 v87, v88, v136
	v_and_b32_e32 v88, 0xffff0000, v205
	v_addc_co_u32_e32 v91, vcc, 0, v171, vcc
	v_fmac_f32_e32 v88, v89, v137
	global_store_dwordx4 v[90:91], v[94:97], off
	v_cvt_pk_bf16_f32 v86, v92, v86
	v_cvt_pk_bf16_f32 v87, v87, v88
	v_lshlrev_b32_e32 v88, 16, v206
	v_fmac_f32_e32 v88, v78, v130
	v_and_b32_e32 v78, 0xffff0000, v206
	v_fmac_f32_e32 v78, v79, v131
	v_cvt_pk_bf16_f32 v88, v88, v78
	v_lshlrev_b32_e32 v78, 16, v207
	v_and_b32_e32 v79, 0xffff0000, v207
	v_fmac_f32_e32 v78, v80, v132
	v_fmac_f32_e32 v79, v81, v133
	v_cvt_pk_bf16_f32 v89, v78, v79
	s_waitcnt vmcnt(6)
	v_lshlrev_b32_e32 v78, 16, v150
	v_and_b32_e32 v79, 0xffff0000, v150
	v_fmac_f32_e32 v78, v82, v142
	v_fmac_f32_e32 v79, v83, v143
	global_store_dwordx4 v[90:91], v[86:89], off offset:256
	v_cvt_pk_bf16_f32 v78, v78, v79
	v_lshlrev_b32_e32 v79, 16, v151
	v_and_b32_e32 v80, 0xffff0000, v151
	v_fmac_f32_e32 v79, v84, v144
	v_fmac_f32_e32 v80, v85, v145
	v_cvt_pk_bf16_f32 v79, v79, v80
	v_lshlrev_b32_e32 v80, 16, v152
	v_fmac_f32_e32 v80, v74, v138
	v_and_b32_e32 v74, 0xffff0000, v152
	v_fmac_f32_e32 v74, v75, v139
	v_cvt_pk_bf16_f32 v80, v80, v74
	v_lshlrev_b32_e32 v74, 16, v153
	v_fmac_f32_e32 v74, v76, v140
	s_waitcnt vmcnt(6)
	v_lshlrev_b32_e32 v76, 16, v146
	v_fmac_f32_e32 v76, v70, v134
	v_and_b32_e32 v70, 0xffff0000, v146
	v_and_b32_e32 v75, 0xffff0000, v153
	v_fmac_f32_e32 v70, v71, v135
	v_lshlrev_b32_e32 v71, 16, v147
	v_fmac_f32_e32 v75, v77, v141
	v_cvt_pk_bf16_f32 v81, v74, v75
	v_add_co_u32_e32 v74, vcc, s41, v170
	v_fmac_f32_e32 v71, v72, v136
	v_and_b32_e32 v72, 0xffff0000, v147
	v_addc_co_u32_e32 v75, vcc, 0, v171, vcc
	v_fmac_f32_e32 v72, v73, v137
	global_store_dwordx4 v[74:75], v[78:81], off
	v_cvt_pk_bf16_f32 v70, v76, v70
	v_cvt_pk_bf16_f32 v71, v71, v72
	v_lshlrev_b32_e32 v72, 16, v148
	v_fmac_f32_e32 v72, v66, v130
	v_and_b32_e32 v66, 0xffff0000, v148
	v_fmac_f32_e32 v66, v67, v131
	v_cvt_pk_bf16_f32 v72, v72, v66
	v_lshlrev_b32_e32 v66, 16, v149
	v_fmac_f32_e32 v66, v68, v132
	v_and_b32_e32 v67, 0xffff0000, v149
	v_fmac_f32_e32 v67, v69, v133
	v_cvt_pk_bf16_f32 v73, v66, v67
	global_store_dwordx4 v[74:75], v[70:73], off offset:256
	s_nop 1
	s_waitcnt vmcnt(8)
; __device__ __forceinline__ unsigned cvt_pk_bf16(float lo, float hi) { unsigned r; asm volatile("v_cvt_pk_bf16_f32 %0, %1, %2" : "=v"(r) : "v"(lo), "v"(hi)); return r; }
;     __device__ __forceinline__ void operator()(const f32x4 (&acc)[2][2][4][2], const Unit& u, int wr, int wc, int fr, int fq) const {
;     ...
;                     for (int bj = 0; bj < 2; ++bj) bs[m][bj] = *(const u32x4*)(bp + (size_t)(ai * HALF + m * 16) * 2048 + bj * HALF);
; #pragma unroll
;                 for (int m = 0; m < 4; ++m)
; #pragma unroll
;                     for (int bj = 0; bj < 2; ++bj) { const u32x4 b = bs[m][bj]; const f32x4 a0 = acc[ai][bj][m][0], a1 = acc[ai][bj][m][1], g0 = gv[bj][0], g1 = gv[bj][1];
;                         u32x4 w;
;                         w.x = cvt_pk_bf16(__builtin_bit_cast(float, b.x << 16) + g0[0] * a0[0], __builtin_bit_cast(float, b.x & 0xffff0000u) + g0[1] * a0[1]);
;                         w.y = cvt_pk_bf16(__builtin_bit_cast(float, b.y << 16) + g0[2] * a0[2], __builtin_bit_cast(float, b.y & 0xffff0000u) + g0[3] * a0[3]);
;                         w.z = cvt_pk_bf16(__builtin_bit_cast(float, b.z << 16) + g1[0] * a1[0], __builtin_bit_cast(float, b.z & 0xffff0000u) + g1[1] * a1[1]);
;                         w.w = cvt_pk_bf16(__builtin_bit_cast(float, b.w << 16) + g1[2] * a1[2], __builtin_bit_cast(float, b.w & 0xffff0000u) + g1[3] * a1[3]);
;                         *(u32x4*)(op + (size_t)(ai * HALF + m * 16) * 2048 + bj * HALF) = w; }
	v_lshlrev_b32_e32 v98, 16, v222
	v_fmac_f32_e32 v98, v62, v142
	s_nop 0
	v_add_co_u32_e32 v66, vcc, s48, v172
	v_and_b32_e32 v62, 0xffff0000, v222
	s_nop 0
	v_addc_co_u32_e32 v67, vcc, 0, v173, vcc
	s_nop 0
	global_load_dwordx4 v[66:69], v[66:67], off offset:256
	v_fmac_f32_e32 v62, v63, v143
	v_lshlrev_b32_e32 v63, 16, v223
	v_fmac_f32_e32 v63, v64, v144
	v_and_b32_e32 v64, 0xffff0000, v223
	v_fmac_f32_e32 v64, v65, v145
	v_cvt_pk_bf16_f32 v62, v98, v62
	v_cvt_pk_bf16_f32 v63, v63, v64
	v_lshlrev_b32_e32 v64, 16, v224
	v_fmac_f32_e32 v64, v58, v138
	v_and_b32_e32 v58, 0xffff0000, v224
	v_fmac_f32_e32 v58, v59, v139
	v_cvt_pk_bf16_f32 v64, v64, v58
	v_lshlrev_b32_e32 v58, 16, v225
	v_fmac_f32_e32 v58, v60, v140
	v_lshlrev_b32_e32 v60, 16, v226
	v_fmac_f32_e32 v60, v54, v134
	v_and_b32_e32 v54, 0xffff0000, v226
	v_and_b32_e32 v59, 0xffff0000, v225
	v_fmac_f32_e32 v54, v55, v135
	v_lshlrev_b32_e32 v55, 16, v227
	v_fmac_f32_e32 v59, v61, v141
	v_cvt_pk_bf16_f32 v65, v58, v59
	v_add_co_u32_e32 v58, vcc, s45, v170
	v_fmac_f32_e32 v55, v56, v136
	v_and_b32_e32 v56, 0xffff0000, v227
	v_addc_co_u32_e32 v59, vcc, 0, v171, vcc
	v_fmac_f32_e32 v56, v57, v137
	global_store_dwordx4 v[58:59], v[62:65], off
	v_cvt_pk_bf16_f32 v54, v60, v54
	v_cvt_pk_bf16_f32 v55, v55, v56
	v_lshlrev_b32_e32 v56, 16, v228
	v_fmac_f32_e32 v56, v46, v130
	v_and_b32_e32 v46, 0xffff0000, v228
	v_fmac_f32_e32 v46, v47, v131
	v_cvt_pk_bf16_f32 v56, v56, v46
	v_lshlrev_b32_e32 v46, 16, v229
	v_and_b32_e32 v47, 0xffff0000, v229
	v_fmac_f32_e32 v46, v48, v132
	v_fmac_f32_e32 v47, v49, v133
	v_cvt_pk_bf16_f32 v57, v46, v47
	global_store_dwordx4 v[58:59], v[54:57], off offset:256
	v_lshlrev_b32_e32 v46, 16, v230
	v_and_b32_e32 v47, 0xffff0000, v230
	v_fmac_f32_e32 v46, v50, v142
	v_fmac_f32_e32 v47, v51, v143
	v_cvt_pk_bf16_f32 v46, v46, v47
	v_lshlrev_b32_e32 v47, 16, v231
	v_and_b32_e32 v48, 0xffff0000, v231
	v_fmac_f32_e32 v47, v52, v144
	v_fmac_f32_e32 v48, v53, v145
	v_cvt_pk_bf16_f32 v47, v47, v48
	v_lshlrev_b32_e32 v48, 16, v232
	v_fmac_f32_e32 v48, v42, v138
	v_and_b32_e32 v42, 0xffff0000, v232
	v_fmac_f32_e32 v42, v43, v139
	v_cvt_pk_bf16_f32 v48, v48, v42
	v_lshlrev_b32_e32 v42, 16, v233
	v_fmac_f32_e32 v42, v44, v140
	v_lshlrev_b32_e32 v44, 16, v234
	v_fmac_f32_e32 v44, v38, v134
	v_and_b32_e32 v38, 0xffff0000, v234
	v_and_b32_e32 v43, 0xffff0000, v233
	v_fmac_f32_e32 v38, v39, v135
	v_lshlrev_b32_e32 v39, 16, v235
	v_fmac_f32_e32 v43, v45, v141
	v_cvt_pk_bf16_f32 v49, v42, v43
	v_add_co_u32_e32 v42, vcc, s46, v170
	v_fmac_f32_e32 v39, v40, v136
	v_and_b32_e32 v40, 0xffff0000, v235
	v_addc_co_u32_e32 v43, vcc, 0, v171, vcc
	v_fmac_f32_e32 v40, v41, v137
	global_store_dwordx4 v[42:43], v[46:49], off
	v_cvt_pk_bf16_f32 v38, v44, v38
	v_cvt_pk_bf16_f32 v39, v39, v40
	v_lshlrev_b32_e32 v40, 16, v236
	v_fmac_f32_e32 v40, v30, v130
	v_and_b32_e32 v30, 0xffff0000, v236
	v_fmac_f32_e32 v30, v31, v131
	v_cvt_pk_bf16_f32 v40, v40, v30
	v_lshlrev_b32_e32 v30, 16, v237
	v_and_b32_e32 v31, 0xffff0000, v237
	v_fmac_f32_e32 v30, v32, v132
	v_fmac_f32_e32 v31, v33, v133
	v_cvt_pk_bf16_f32 v41, v30, v31
	v_lshlrev_b32_e32 v30, 16, v238
	v_and_b32_e32 v31, 0xffff0000, v238
	v_fmac_f32_e32 v30, v34, v142
	v_fmac_f32_e32 v31, v35, v143
	global_store_dwordx4 v[42:43], v[38:41], off offset:256
	v_cvt_pk_bf16_f32 v30, v30, v31
	v_lshlrev_b32_e32 v31, 16, v239
	v_and_b32_e32 v32, 0xffff0000, v239
	v_fmac_f32_e32 v31, v36, v144
	v_fmac_f32_e32 v32, v37, v145
	v_cvt_pk_bf16_f32 v31, v31, v32
	v_lshlrev_b32_e32 v32, 16, v240
	v_fmac_f32_e32 v32, v26, v138
	v_and_b32_e32 v26, 0xffff0000, v240
	v_fmac_f32_e32 v26, v27, v139
	v_cvt_pk_bf16_f32 v32, v32, v26
	v_lshlrev_b32_e32 v26, 16, v241
	v_fmac_f32_e32 v26, v28, v140
	v_lshlrev_b32_e32 v28, 16, v242
	v_fmac_f32_e32 v28, v22, v134
	v_and_b32_e32 v22, 0xffff0000, v242
	v_and_b32_e32 v27, 0xffff0000, v241
	v_fmac_f32_e32 v22, v23, v135
	v_lshlrev_b32_e32 v23, 16, v243
	v_fmac_f32_e32 v27, v29, v141
	v_cvt_pk_bf16_f32 v33, v26, v27
	v_add_co_u32_e32 v26, vcc, s47, v170
	v_fmac_f32_e32 v23, v24, v136
	v_and_b32_e32 v24, 0xffff0000, v243
	v_addc_co_u32_e32 v27, vcc, 0, v171, vcc
	v_fmac_f32_e32 v24, v25, v137
	global_store_dwordx4 v[26:27], v[30:33], off
	v_cvt_pk_bf16_f32 v22, v28, v22
	v_cvt_pk_bf16_f32 v23, v23, v24
	v_lshlrev_b32_e32 v24, 16, v244
	v_fmac_f32_e32 v24, v14, v130
	v_and_b32_e32 v14, 0xffff0000, v244
	v_fmac_f32_e32 v14, v15, v131
	v_cvt_pk_bf16_f32 v24, v24, v14
	v_lshlrev_b32_e32 v14, 16, v245
	v_and_b32_e32 v15, 0xffff0000, v245
	v_fmac_f32_e32 v14, v16, v132
	v_fmac_f32_e32 v15, v17, v133
	v_cvt_pk_bf16_f32 v25, v14, v15
	v_lshlrev_b32_e32 v14, 16, v250
	v_and_b32_e32 v15, 0xffff0000, v250
	v_fmac_f32_e32 v14, v18, v142
	v_fmac_f32_e32 v15, v19, v143
	global_store_dwordx4 v[26:27], v[22:25], off offset:256
	v_cvt_pk_bf16_f32 v14, v14, v15
	v_lshlrev_b32_e32 v15, 16, v251
	v_and_b32_e32 v16, 0xffff0000, v251
	v_fmac_f32_e32 v15, v20, v144
	v_fmac_f32_e32 v16, v21, v145
	v_cvt_pk_bf16_f32 v15, v15, v16
	v_lshlrev_b32_e32 v16, 16, v252
	v_fmac_f32_e32 v16, v10, v138
	v_and_b32_e32 v10, 0xffff0000, v252
	v_fmac_f32_e32 v10, v11, v139
	v_cvt_pk_bf16_f32 v16, v16, v10
	v_lshlrev_b32_e32 v10, 16, v253
	v_fmac_f32_e32 v10, v12, v140
	s_waitcnt vmcnt(6)
	v_lshlrev_b32_e32 v12, 16, v66
	v_fmac_f32_e32 v12, v6, v134
	v_and_b32_e32 v6, 0xffff0000, v66
	v_and_b32_e32 v11, 0xffff0000, v253
	v_fmac_f32_e32 v6, v7, v135
	v_lshlrev_b32_e32 v7, 16, v67
	v_fmac_f32_e32 v11, v13, v141
	v_cvt_pk_bf16_f32 v17, v10, v11
	v_add_co_u32_e32 v10, vcc, s48, v170
	v_fmac_f32_e32 v7, v8, v136
	v_and_b32_e32 v8, 0xffff0000, v67
	v_addc_co_u32_e32 v11, vcc, 0, v171, vcc
	v_fmac_f32_e32 v8, v9, v137
	global_store_dwordx4 v[10:11], v[14:17], off
	v_cvt_pk_bf16_f32 v6, v12, v6
	v_cvt_pk_bf16_f32 v7, v7, v8
	v_lshlrev_b32_e32 v8, 16, v68
	v_fmac_f32_e32 v8, v2, v130
	v_and_b32_e32 v2, 0xffff0000, v68
	v_fmac_f32_e32 v2, v3, v131
	v_cvt_pk_bf16_f32 v8, v8, v2
	v_lshlrev_b32_e32 v2, 16, v69
	v_and_b32_e32 v3, 0xffff0000, v69
	v_fmac_f32_e32 v2, v4, v132
	v_fmac_f32_e32 v3, v5, v133
	v_cvt_pk_bf16_f32 v9, v2, v3
	global_store_dwordx4 v[10:11], v[6:9], off offset:256
	s_andn2_b64 vcc, exec, s[2:3]
	s_mov_b64 s[2:3], -1
	s_cbranch_vccnz .LBB0_1448
	s_andn2_b64 vcc, exec, s[4:5]
	s_cbranch_vccnz .LBB0_1447
	s_barrier
	s_branch .LBB0_1447
